# batch7: + P5 head epilogue hand-scheduled (interleaved silu chains, no packed multiplies or pads)
# speedup vs baseline: 1.0081x; 1.0081x over previous
.Lp5_zw_done:
	v_exp_f32_e32 v107, v106
	v_lshlrev_b32_e32 v106, 16, v74
	v_and_b32_e32 v108, 0xffff0000, v74
	v_mul_f32_e32 v109, 0xbfb8aa3b, v106
	v_mul_f32_e32 v74, 0xbfb8aa3b, v108
	v_exp_f32_e32 v109, v109
	v_exp_f32_e32 v74, v74
	v_fma_f32 v90, v107, v132, v90
	v_fma_f32 v91, v107, v133, v91
	v_add_f32_e32 v109, 1.0, v109
	v_add_f32_e32 v74, 1.0, v74
	v_rcp_f32_e32 v109, v109
	v_rcp_f32_e32 v74, v74
	v_mul_f32_e32 v90, v90, v106
	v_mul_f32_e32 v91, v91, v108
	v_mul_f32_e32 v90, v90, v109
	v_mul_f32_e32 v91, v91, v74
	v_lshlrev_b32_e32 v106, 16, v75
	v_and_b32_e32 v108, 0xffff0000, v75
	v_mul_f32_e32 v109, 0xbfb8aa3b, v106
	v_mul_f32_e32 v75, 0xbfb8aa3b, v108
	v_exp_f32_e32 v109, v109
	v_exp_f32_e32 v75, v75
	v_fma_f32 v92, v107, v134, v92
	v_fma_f32 v93, v107, v135, v93
	v_add_f32_e32 v109, 1.0, v109
	v_add_f32_e32 v75, 1.0, v75
	v_rcp_f32_e32 v109, v109
	v_rcp_f32_e32 v75, v75
	v_mul_f32_e32 v92, v92, v106
	v_mul_f32_e32 v93, v93, v108
	v_mul_f32_e32 v92, v92, v109
	v_mul_f32_e32 v93, v93, v75
	v_lshlrev_b32_e32 v106, 16, v76
	v_and_b32_e32 v108, 0xffff0000, v76
	v_mul_f32_e32 v109, 0xbfb8aa3b, v106
	v_mul_f32_e32 v76, 0xbfb8aa3b, v108
	v_exp_f32_e32 v109, v109
	v_exp_f32_e32 v76, v76
	v_fma_f32 v86, v107, v102, v86
	v_fma_f32 v87, v107, v103, v87
	v_add_f32_e32 v109, 1.0, v109
	v_add_f32_e32 v76, 1.0, v76
	v_rcp_f32_e32 v109, v109
	v_rcp_f32_e32 v76, v76
	v_mul_f32_e32 v86, v86, v106
	v_mul_f32_e32 v87, v87, v108
	v_mul_f32_e32 v86, v86, v109
	v_mul_f32_e32 v87, v87, v76
	v_lshlrev_b32_e32 v106, 16, v77
	v_and_b32_e32 v108, 0xffff0000, v77
	v_mul_f32_e32 v109, 0xbfb8aa3b, v106
	v_mul_f32_e32 v77, 0xbfb8aa3b, v108
	v_exp_f32_e32 v109, v109
	v_exp_f32_e32 v77, v77
	v_fma_f32 v88, v107, v104, v88
	v_fma_f32 v89, v107, v105, v89
	v_add_f32_e32 v109, 1.0, v109
	v_add_f32_e32 v77, 1.0, v77
	v_rcp_f32_e32 v109, v109
	v_rcp_f32_e32 v77, v77
	v_mul_f32_e32 v88, v88, v106
	v_mul_f32_e32 v89, v89, v108
	v_mul_f32_e32 v88, v88, v109
	v_mul_f32_e32 v89, v89, v77
	v_cvt_pk_bf16_f32 v74, v90, v91
	v_cvt_pk_bf16_f32 v75, v92, v93
	v_cvt_pk_bf16_f32 v76, v86, v87
	v_cvt_pk_bf16_f32 v77, v88, v89
	s_cmp_gt_u32 s2, 3
	s_cselect_b64 s[6:7], -1, 0
	s_cmp_lt_u32 s2, 2
	s_cselect_b64 s[88:89], -1, 0
	s_mov_b64 s[8:9], -1
	s_and_b64 vcc, exec, s[6:7]
	s_cbranch_vccz .LBB0_576
	v_add_co_u32_e32 v102, vcc, 0x66100000, v128
	s_mov_b64 s[8:9], 0
	s_nop 0
	v_addc_co_u32_e32 v103, vcc, 0, v129, vcc
	global_store_dwordx4 v[102:103], v[74:77], off

.LBB0_578:
	s_waitcnt vmcnt(0)
	v_lshlrev_b32_e32 v106, 16, v70
	v_and_b32_e32 v108, 0xffff0000, v70
	v_mul_f32_e32 v109, 0xbfb8aa3b, v106
	v_mul_f32_e32 v70, 0xbfb8aa3b, v108
	v_exp_f32_e32 v109, v109
	v_exp_f32_e32 v70, v70
	v_fma_f32 v82, v107, v98, v82
	v_fma_f32 v83, v107, v99, v83
	v_add_f32_e32 v109, 1.0, v109
	v_add_f32_e32 v70, 1.0, v70
	v_rcp_f32_e32 v109, v109
	v_rcp_f32_e32 v70, v70
	v_mul_f32_e32 v82, v82, v106
	v_mul_f32_e32 v83, v83, v108
	v_mul_f32_e32 v82, v82, v109
	v_mul_f32_e32 v83, v83, v70
	v_lshlrev_b32_e32 v106, 16, v71
	v_and_b32_e32 v108, 0xffff0000, v71
	v_mul_f32_e32 v109, 0xbfb8aa3b, v106
	v_mul_f32_e32 v71, 0xbfb8aa3b, v108
	v_exp_f32_e32 v109, v109
	v_exp_f32_e32 v71, v71
	v_fma_f32 v84, v107, v100, v84
	v_fma_f32 v85, v107, v101, v85
	v_add_f32_e32 v109, 1.0, v109
	v_add_f32_e32 v71, 1.0, v71
	v_rcp_f32_e32 v109, v109
	v_rcp_f32_e32 v71, v71
	v_mul_f32_e32 v84, v84, v106
	v_mul_f32_e32 v85, v85, v108
	v_mul_f32_e32 v84, v84, v109
	v_mul_f32_e32 v85, v85, v71
	v_lshlrev_b32_e32 v106, 16, v72
	v_and_b32_e32 v108, 0xffff0000, v72
	v_mul_f32_e32 v109, 0xbfb8aa3b, v106
	v_mul_f32_e32 v72, 0xbfb8aa3b, v108
	v_exp_f32_e32 v109, v109
	v_exp_f32_e32 v72, v72
	v_fma_f32 v78, v107, v94, v78
	v_fma_f32 v94, v107, v95, v79
	v_add_f32_e32 v109, 1.0, v109
	v_add_f32_e32 v72, 1.0, v72
	v_rcp_f32_e32 v109, v109
	v_rcp_f32_e32 v72, v72
	v_mul_f32_e32 v78, v78, v106
	v_mul_f32_e32 v94, v94, v108
	v_mul_f32_e32 v78, v78, v109
	v_mul_f32_e32 v94, v94, v72
	v_lshlrev_b32_e32 v106, 16, v73
	v_and_b32_e32 v108, 0xffff0000, v73
	v_mul_f32_e32 v109, 0xbfb8aa3b, v106
	v_mul_f32_e32 v73, 0xbfb8aa3b, v108
	v_exp_f32_e32 v109, v109
	v_exp_f32_e32 v73, v73
	v_fma_f32 v79, v107, v96, v80
	v_fma_f32 v80, v107, v97, v81
	v_add_f32_e32 v109, 1.0, v109
	v_add_f32_e32 v73, 1.0, v73
	v_rcp_f32_e32 v109, v109
	v_rcp_f32_e32 v73, v73
	v_mul_f32_e32 v79, v79, v106
	v_mul_f32_e32 v80, v80, v108
	v_mul_f32_e32 v79, v79, v109
	v_mul_f32_e32 v80, v80, v73
	v_cvt_pk_bf16_f32 v70, v82, v83
	v_cvt_pk_bf16_f32 v71, v84, v85
	v_cvt_pk_bf16_f32 v72, v78, v94
	v_cvt_pk_bf16_f32 v73, v79, v80
	s_andn2_b64 vcc, exec, s[6:7]
	s_mov_b64 s[6:7], -1
	s_cbranch_vccz .LBB0_596
	s_andn2_b64 vcc, exec, s[6:7]
	s_cbranch_vccz .LBB0_597
